# speedup vs baseline: 1.0024x; 1.0024x over previous
.LBB3_9:
	ds_read_b128 v[146:149], v150
	ds_read_b128 v[156:159], v150 offset:2048
	ds_read_b128 v[170:173], v154
	ds_read_b128 v[174:177], v154 offset:2048
	s_mov_b32 s65, s54
	s_mov_b32 s54, s66
	ds_read_b128 v[138:141], v163
	ds_read_b128 v[126:129], v163 offset:2048
	ds_read_b128 v[142:145], v164
	ds_read_b128 v[130:133], v164 offset:2048
	ds_read_b128 v[122:125], v163 offset:4096
	ds_read_b128 v[114:117], v163 offset:6144
	ds_read_b128 v[134:137], v164 offset:4096
	ds_read_b128 v[118:121], v164 offset:6144
	s_waitcnt vmcnt(10)
	s_mul_i32 s21, s52, s22
	s_lshl_b32 s20, s27, 6
	v_add_u32_e32 v169, s65, v1
	ds_write_b128 v1, v[22:25] offset:16384
	ds_write_b128 v1, v[18:21] offset:24576
	s_nop 0
	s_add_i32 s66, s21, s20
	s_lshl_b32 s66, s66, 1
	s_add_i32 s67, s66, s51
	buffer_load_dwordx4 v[22:25], v162, s[0:3], s66 offen
	buffer_load_dwordx4 v[18:21], v162, s[0:3], s67 offen
	s_waitcnt vmcnt(10)
	ds_write_b128 v169, v[14:17] offset:32768
	ds_write_b128 v169, v[10:13] offset:40960
	s_nop 0
	s_mul_i32 s66, s53, s22
	s_add_i32 s67, s66, s20
	s_lshl_b32 s67, s67, 1
	s_add_i32 s68, s67, s51
	s_nop 4
	buffer_load_dwordx4 v[14:17], v162, s[28:31], s67 offen
	buffer_load_dwordx4 v[10:13], v162, s[28:31], s68 offen
	s_barrier
	s_setprio 1
	s_waitcnt lgkmcnt(11)
	v_mfma_f32_16x16x32_f16 v[110:113], v[146:149], v[138:141], v[110:113]
	v_mfma_f32_16x16x32_f16 v[106:109], v[156:159], v[138:141], v[106:109]
	s_waitcnt lgkmcnt(10)
	v_mfma_f32_16x16x32_f16 v[102:105], v[146:149], v[126:129], v[102:105]
	v_mfma_f32_16x16x32_f16 v[98:101], v[156:159], v[126:129], v[98:101]
	s_waitcnt lgkmcnt(7)
	v_mfma_f32_16x16x32_f16 v[94:97], v[146:149], v[122:125], v[94:97]
	v_mfma_f32_16x16x32_f16 v[90:93], v[156:159], v[122:125], v[90:93]
	s_waitcnt lgkmcnt(6)
	v_mfma_f32_16x16x32_f16 v[86:89], v[146:149], v[114:117], v[86:89]
	v_mfma_f32_16x16x32_f16 v[82:85], v[156:159], v[114:117], v[82:85]
	v_mfma_f32_16x16x32_f16 v[110:113], v[170:173], v[142:145], v[110:113]
	v_mfma_f32_16x16x32_f16 v[106:109], v[174:177], v[142:145], v[106:109]
	v_mfma_f32_16x16x32_f16 v[102:105], v[170:173], v[130:133], v[102:105]
	v_mfma_f32_16x16x32_f16 v[98:101], v[174:177], v[130:133], v[98:101]
	s_waitcnt lgkmcnt(5)
	v_mfma_f32_16x16x32_f16 v[94:97], v[170:173], v[134:137], v[94:97]
	v_mfma_f32_16x16x32_f16 v[90:93], v[174:177], v[134:137], v[90:93]
	s_waitcnt lgkmcnt(4)
	v_mfma_f32_16x16x32_f16 v[86:89], v[170:173], v[118:121], v[86:89]
	v_mfma_f32_16x16x32_f16 v[82:85], v[174:177], v[118:121], v[82:85]
	s_waitcnt lgkmcnt(0)
	s_setprio 0
	s_barrier
	ds_read_b128 v[146:149], v150 offset:16384
	ds_read_b128 v[150:153], v150 offset:18432
	ds_read_b128 v[158:161], v154 offset:16384
	ds_read_b128 v[154:157], v154 offset:18432
	s_waitcnt vmcnt(10)
	s_add_i32 s67, s66, s51
	s_add_i32 s20, s67, s20
	s_lshl_b32 s20, s20, 1
	ds_write_b128 v169, v[6:9] offset:49152
	ds_write_b128 v169, v[2:5] offset:57344
	s_add_i32 s68, s20, s51
	s_nop 4
	buffer_load_dwordx4 v[6:9], v162, s[28:31], s20 offen
	buffer_load_dwordx4 v[2:5], v162, s[28:31], s68 offen
	s_add_i32 s27, s27, 1
	s_cmp_eq_u32 s27, s55
	s_cbranch_scc0 .LBB3_13
	s_add_i32 s20, s64, 1
	s_cmp_gt_i32 s64, -1
	s_cbranch_scc1 .LBB3_12
	s_mul_i32 s0, s20, s33
	s_add_i32 s0, s0, s44
	s_abs_i32 s21, s0
	s_mul_hi_u32 s27, s21, s46
	s_mul_i32 s28, s27, s43
	s_ashr_i32 s1, s0, 31
	s_sub_i32 s21, s21, s28
	s_xor_b32 s1, s1, s45
	s_add_i32 s28, s27, 1
	s_sub_i32 s29, s21, s43
	s_cmp_ge_u32 s21, s43
	s_cselect_b32 s27, s28, s27
	s_cselect_b32 s21, s29, s21
	s_add_i32 s28, s27, 1
	s_cmp_ge_u32 s21, s43
	s_cselect_b32 s21, s28, s27
	s_xor_b32 s21, s21, s1
	s_sub_i32 s1, s21, s1
	s_mul_i32 s21, s1, s42
	s_sub_i32 s0, s0, s21
	s_abs_i32 s27, s0
	s_mul_hi_u32 s28, s27, s49
	s_mul_i32 s29, s28, s47
	s_ashr_i32 s21, s0, 31
	s_sub_i32 s27, s27, s29
	s_xor_b32 s21, s21, s48
	s_add_i32 s29, s28, 1
	s_sub_i32 s30, s27, s47
	s_cmp_ge_u32 s27, s47
	s_cselect_b32 s28, s29, s28
	s_cselect_b32 s27, s30, s27
	s_add_i32 s29, s28, 1
	s_cmp_ge_u32 s27, s47
	s_cselect_b32 s27, s29, s28
	s_xor_b32 s27, s27, s21
	s_sub_i32 s21, s27, s21
	s_lshl_b32 s52, s21, 7
	s_mul_i32 s21, s21, s23
	s_sub_i32 s0, s0, s21
	s_lshl_b32 s53, s0, 8
	s_cmp_eq_u32 s1, 1
	s_cselect_b32 s21, s7, s9
	s_cselect_b32 s0, s6, s8
	s_cselect_b32 s27, s13, s15
	s_cselect_b32 s28, s12, s14
	s_cmp_eq_u32 s1, 0
	s_cselect_b32 s1, s5, s21
	s_cselect_b32 s21, s11, s27
	s_mov_b32 s27, s3
	s_mul_i32 s66, s53, s22
	s_cselect_b32 s0, s4, s0
	s_cselect_b32 s28, s10, s28
	s_and_b32 s1, s1, 0xffff
	s_and_b32 s29, s21, 0xffff
	s_mul_i32 s21, s52, s22
	s_add_i32 s67, s66, s51
	s_mov_b64 s[30:31], s[26:27]

.LBB3_14:
	s_barrier
	s_setprio 1
	s_waitcnt lgkmcnt(5)
	v_mfma_f32_16x16x32_f16 v[78:81], v[146:149], v[138:141], v[78:81]
	s_waitcnt lgkmcnt(4)
	v_mfma_f32_16x16x32_f16 v[74:77], v[150:153], v[138:141], v[74:77]
	v_mfma_f32_16x16x32_f16 v[70:73], v[146:149], v[126:129], v[70:73]
	v_mfma_f32_16x16x32_f16 v[66:69], v[150:153], v[126:129], v[66:69]
	v_mfma_f32_16x16x32_f16 v[62:65], v[146:149], v[122:125], v[62:65]
	v_mfma_f32_16x16x32_f16 v[58:61], v[150:153], v[122:125], v[58:61]
	v_mfma_f32_16x16x32_f16 v[54:57], v[146:149], v[114:117], v[54:57]
	v_mfma_f32_16x16x32_f16 v[50:53], v[150:153], v[114:117], v[50:53]
	s_waitcnt lgkmcnt(3)
	v_mfma_f32_16x16x32_f16 v[78:81], v[158:161], v[142:145], v[78:81]
	s_waitcnt lgkmcnt(2)
	v_mfma_f32_16x16x32_f16 v[74:77], v[154:157], v[142:145], v[74:77]
	v_mfma_f32_16x16x32_f16 v[70:73], v[158:161], v[130:133], v[70:73]
	v_mfma_f32_16x16x32_f16 v[66:69], v[154:157], v[130:133], v[66:69]
	v_mfma_f32_16x16x32_f16 v[62:65], v[158:161], v[134:137], v[62:65]
	v_mfma_f32_16x16x32_f16 v[58:61], v[154:157], v[134:137], v[58:61]
	v_mfma_f32_16x16x32_f16 v[54:57], v[158:161], v[118:121], v[54:57]
	v_mfma_f32_16x16x32_f16 v[50:53], v[154:157], v[118:121], v[50:53]
	s_waitcnt lgkmcnt(0)
	s_setprio 0
	s_barrier
	v_add_u32_e32 v169, s65, v165
	v_add_u32_e32 v170, s65, v168
	ds_read_b128 v[146:149], v169 offset:32768
	ds_read_b128 v[150:153], v169 offset:34816
	ds_read_b128 v[154:157], v170 offset:32768
	ds_read_b128 v[158:161], v170 offset:34816
	ds_read_b128 v[138:141], v163 offset:16384
	ds_read_b128 v[126:129], v163 offset:18432
	ds_read_b128 v[142:145], v164 offset:16384
	ds_read_b128 v[130:133], v164 offset:18432
	ds_read_b128 v[122:125], v163 offset:20480
	ds_read_b128 v[114:117], v163 offset:22528
	ds_read_b128 v[134:137], v164 offset:20480
	ds_read_b128 v[118:121], v164 offset:22528
	s_waitcnt vmcnt(10)
	s_lshl_b32 s64, s27, 6
	v_add_u32_e32 v171, s62, v1
	s_add_i32 s21, s21, s64
	ds_write_b128 v1, v[46:49]
	ds_write_b128 v1, v[42:45] offset:8192
	s_nop 0
	s_lshl_b32 s21, s21, 1
	s_add_i32 s68, s21, s51
	buffer_load_dwordx4 v[46:49], v162, s[0:3], s21 offen
	buffer_load_dwordx4 v[42:45], v162, s[0:3], s68 offen
	s_waitcnt vmcnt(10)
	ds_write_b128 v171, v[38:41] offset:32768
	ds_write_b128 v171, v[34:37] offset:40960
	s_nop 0
	s_add_i32 s21, s66, s64
	s_lshl_b32 s21, s21, 1
	s_add_i32 s66, s21, s51
	s_nop 4
	buffer_load_dwordx4 v[38:41], v162, s[28:31], s21 offen
	buffer_load_dwordx4 v[34:37], v162, s[28:31], s66 offen
	s_barrier
	s_setprio 1
	s_waitcnt lgkmcnt(11)
	v_mfma_f32_16x16x32_f16 v[110:113], v[146:149], v[138:141], v[110:113]
	v_mfma_f32_16x16x32_f16 v[106:109], v[150:153], v[138:141], v[106:109]
	s_waitcnt lgkmcnt(10)
	v_mfma_f32_16x16x32_f16 v[102:105], v[146:149], v[126:129], v[102:105]
	v_mfma_f32_16x16x32_f16 v[98:101], v[150:153], v[126:129], v[98:101]
	s_waitcnt lgkmcnt(7)
	v_mfma_f32_16x16x32_f16 v[94:97], v[146:149], v[122:125], v[94:97]
	v_mfma_f32_16x16x32_f16 v[90:93], v[150:153], v[122:125], v[90:93]
	s_waitcnt lgkmcnt(6)
	v_mfma_f32_16x16x32_f16 v[86:89], v[146:149], v[114:117], v[86:89]
	v_mfma_f32_16x16x32_f16 v[82:85], v[150:153], v[114:117], v[82:85]
	v_mfma_f32_16x16x32_f16 v[110:113], v[154:157], v[142:145], v[110:113]
	v_mfma_f32_16x16x32_f16 v[106:109], v[158:161], v[142:145], v[106:109]
	v_mfma_f32_16x16x32_f16 v[102:105], v[154:157], v[130:133], v[102:105]
	v_mfma_f32_16x16x32_f16 v[98:101], v[158:161], v[130:133], v[98:101]
	s_waitcnt lgkmcnt(5)
	v_mfma_f32_16x16x32_f16 v[94:97], v[154:157], v[134:137], v[94:97]
	v_mfma_f32_16x16x32_f16 v[90:93], v[158:161], v[134:137], v[90:93]
	s_waitcnt lgkmcnt(4)
	v_mfma_f32_16x16x32_f16 v[86:89], v[154:157], v[118:121], v[86:89]
	v_mfma_f32_16x16x32_f16 v[82:85], v[158:161], v[118:121], v[82:85]
	s_waitcnt lgkmcnt(0)
	s_setprio 0
	s_barrier
	ds_read_b128 v[146:149], v169 offset:49152
	ds_read_b128 v[150:153], v169 offset:51200
	ds_read_b128 v[158:161], v170 offset:49152
	ds_read_b128 v[154:157], v170 offset:51200
	s_waitcnt vmcnt(10)
	s_add_i32 s21, s67, s64
	s_lshl_b32 s21, s21, 1
	s_add_i32 s64, s21, s51
	ds_write_b128 v171, v[30:33] offset:49152
	ds_write_b128 v171, v[26:29] offset:57344
	s_nop 4
	buffer_load_dwordx4 v[30:33], v162, s[28:31], s21 offen
	buffer_load_dwordx4 v[26:29], v162, s[28:31], s64 offen
	s_add_i32 s27, s27, 1
	s_cmp_lg_u32 s27, s55
	s_cbranch_scc1 .LBB3_18
	s_add_i32 s64, s20, 1
	s_cmp_gt_i32 s20, -1
	s_cbranch_scc1 .LBB3_17
	s_mul_i32 s0, s64, s33
	s_add_i32 s0, s0, s44
	s_abs_i32 s20, s0
	s_mul_hi_u32 s21, s20, s46
	s_mul_i32 s27, s21, s43
	s_ashr_i32 s1, s0, 31
	s_sub_i32 s20, s20, s27
	s_xor_b32 s1, s1, s45
	s_add_i32 s27, s21, 1
	s_sub_i32 s28, s20, s43
	s_cmp_ge_u32 s20, s43
	s_cselect_b32 s21, s27, s21
	s_cselect_b32 s20, s28, s20
	s_add_i32 s27, s21, 1
	s_cmp_ge_u32 s20, s43
	s_cselect_b32 s20, s27, s21
	s_xor_b32 s20, s20, s1
	s_sub_i32 s1, s20, s1
	s_mul_i32 s20, s1, s42
	s_sub_i32 s0, s0, s20
	s_abs_i32 s21, s0
	s_mul_hi_u32 s27, s21, s49
	s_mul_i32 s28, s27, s47
	s_ashr_i32 s20, s0, 31
	s_sub_i32 s21, s21, s28
	s_xor_b32 s20, s20, s48
	s_add_i32 s28, s27, 1
	s_sub_i32 s29, s21, s47
	s_cmp_ge_u32 s21, s47
	s_cselect_b32 s27, s28, s27
	s_cselect_b32 s21, s29, s21
	s_add_i32 s28, s27, 1
	s_cmp_ge_u32 s21, s47
	s_cselect_b32 s21, s28, s27
	s_xor_b32 s21, s21, s20
	s_sub_i32 s20, s21, s20
	s_lshl_b32 s52, s20, 7
	s_mul_i32 s20, s20, s23
	s_sub_i32 s0, s0, s20
	s_lshl_b32 s53, s0, 8
	s_cmp_eq_u32 s1, 1
	s_cselect_b32 s20, s7, s9
	s_cselect_b32 s0, s6, s8
	s_cselect_b32 s21, s13, s15
	s_cselect_b32 s27, s12, s14
	s_cmp_eq_u32 s1, 0
	s_cselect_b32 s1, s5, s20
	s_cselect_b32 s28, s10, s27
	s_cselect_b32 s20, s11, s21
	s_mov_b32 s27, s3
	s_cselect_b32 s0, s4, s0
	s_and_b32 s1, s1, 0xffff
	s_and_b32 s29, s20, 0xffff
	s_mov_b64 s[30:31], s[26:27]

.LBB3_19:
	s_barrier
	s_setprio 1
	s_waitcnt lgkmcnt(5)
	v_mfma_f32_16x16x32_f16 v[78:81], v[146:149], v[138:141], v[78:81]
	s_waitcnt lgkmcnt(4)
	v_mfma_f32_16x16x32_f16 v[74:77], v[150:153], v[138:141], v[74:77]
	v_mfma_f32_16x16x32_f16 v[70:73], v[146:149], v[126:129], v[70:73]
	v_mfma_f32_16x16x32_f16 v[66:69], v[150:153], v[126:129], v[66:69]
	v_mfma_f32_16x16x32_f16 v[62:65], v[146:149], v[122:125], v[62:65]
	v_mfma_f32_16x16x32_f16 v[58:61], v[150:153], v[122:125], v[58:61]
	v_mfma_f32_16x16x32_f16 v[54:57], v[146:149], v[114:117], v[54:57]
	v_mfma_f32_16x16x32_f16 v[50:53], v[150:153], v[114:117], v[50:53]
	s_waitcnt lgkmcnt(3)
	v_mfma_f32_16x16x32_f16 v[78:81], v[158:161], v[142:145], v[78:81]
	s_waitcnt lgkmcnt(2)
	v_mfma_f32_16x16x32_f16 v[74:77], v[154:157], v[142:145], v[74:77]
	v_mfma_f32_16x16x32_f16 v[70:73], v[158:161], v[130:133], v[70:73]
	v_mfma_f32_16x16x32_f16 v[66:69], v[154:157], v[130:133], v[66:69]
	v_mfma_f32_16x16x32_f16 v[62:65], v[158:161], v[134:137], v[62:65]
	v_mfma_f32_16x16x32_f16 v[58:61], v[154:157], v[134:137], v[58:61]
	v_mfma_f32_16x16x32_f16 v[54:57], v[158:161], v[118:121], v[54:57]
	v_mfma_f32_16x16x32_f16 v[50:53], v[154:157], v[118:121], v[50:53]
	s_waitcnt lgkmcnt(0)
	s_setprio 0
	s_barrier
	s_add_i32 s66, s63, 2
	s_cmp_eq_u32 s66, s55
	s_cselect_b64 s[20:21], -1, 0
	s_cmp_lg_u32 s66, s55
	s_cbranch_scc1 .LBB3_8
	buffer_store_dwordx4 v[110:113], v0, s[16:19], s24 offen
	buffer_store_dwordx4 v[106:109], v0, s[16:19], s25 offen
	buffer_store_dwordx4 v[102:105], v0, s[16:19], s34 offen
	buffer_store_dwordx4 v[98:101], v0, s[16:19], s35 offen
	buffer_store_dwordx4 v[94:97], v0, s[16:19], s36 offen
	buffer_store_dwordx4 v[90:93], v0, s[16:19], s37 offen
	buffer_store_dwordx4 v[86:89], v0, s[16:19], s38 offen
	buffer_store_dwordx4 v[82:85], v0, s[16:19], s39 offen
	buffer_store_dwordx4 v[78:81], v0, s[16:19], s40 offen
	buffer_store_dwordx4 v[74:77], v0, s[16:19], s41 offen
	buffer_store_dwordx4 v[70:73], v0, s[16:19], s56 offen
	buffer_store_dwordx4 v[66:69], v0, s[16:19], s57 offen
	buffer_store_dwordx4 v[62:65], v0, s[16:19], s58 offen
	buffer_store_dwordx4 v[58:61], v0, s[16:19], s59 offen
	buffer_store_dwordx4 v[54:57], v0, s[16:19], s60 offen
	buffer_store_dwordx4 v[50:53], v0, s[16:19], s61 offen
	v_mov_b32_e32 v50, 0
	s_mov_b32 s63, -2
	v_mov_b32_e32 v51, v50
	v_mov_b32_e32 v52, v50
	v_mov_b32_e32 v53, v50
	v_mov_b32_e32 v54, v50
	v_mov_b32_e32 v55, v50
	v_mov_b32_e32 v56, v50
	v_mov_b32_e32 v57, v50
	v_mov_b32_e32 v58, v50
	v_mov_b32_e32 v59, v50
	v_mov_b32_e32 v60, v50
	v_mov_b32_e32 v61, v50
	v_mov_b32_e32 v62, v50
	v_mov_b32_e32 v63, v50
	v_mov_b32_e32 v64, v50
	v_mov_b32_e32 v65, v50
	v_mov_b32_e32 v66, v50
	v_mov_b32_e32 v67, v50
	v_mov_b32_e32 v68, v50
	v_mov_b32_e32 v69, v50
	v_mov_b32_e32 v70, v50
	v_mov_b32_e32 v71, v50
	v_mov_b32_e32 v72, v50
	v_mov_b32_e32 v73, v50
	v_mov_b32_e32 v74, v50
	v_mov_b32_e32 v75, v50
	v_mov_b32_e32 v76, v50
	v_mov_b32_e32 v77, v50
	v_mov_b32_e32 v78, v50
	v_mov_b32_e32 v79, v50
	v_mov_b32_e32 v80, v50
	v_mov_b32_e32 v81, v50
	v_mov_b32_e32 v82, v50
	v_mov_b32_e32 v83, v50
	v_mov_b32_e32 v84, v50
	v_mov_b32_e32 v85, v50
	v_mov_b32_e32 v86, v50
	v_mov_b32_e32 v87, v50
	v_mov_b32_e32 v88, v50
	v_mov_b32_e32 v89, v50
	v_mov_b32_e32 v90, v50
	v_mov_b32_e32 v91, v50
	v_mov_b32_e32 v92, v50
	v_mov_b32_e32 v93, v50
	v_mov_b32_e32 v94, v50
	v_mov_b32_e32 v95, v50
	v_mov_b32_e32 v96, v50
	v_mov_b32_e32 v97, v50
	v_mov_b32_e32 v98, v50
	v_mov_b32_e32 v99, v50
	v_mov_b32_e32 v100, v50
	v_mov_b32_e32 v101, v50
	v_mov_b32_e32 v102, v50
	v_mov_b32_e32 v103, v50
	v_mov_b32_e32 v104, v50
	v_mov_b32_e32 v105, v50
	v_mov_b32_e32 v106, v50
	v_mov_b32_e32 v107, v50
	v_mov_b32_e32 v108, v50
	v_mov_b32_e32 v109, v50
	v_mov_b32_e32 v110, v50
	v_mov_b32_e32 v111, v50
	v_mov_b32_e32 v112, v50
	v_mov_b32_e32 v113, v50
	s_branch .LBB3_8
